# lean attention loop (pair-wait, lookahead 8) with the full per-tile priority alternation
# baseline (speedup 1.0000x reference)
.Lattn_pb0:
	s_waitcnt lgkmcnt(6)
	v_mfma_f32_16x16x32_bf16 v[64:67], v[160:163], v[96:99], 0
	v_exp_f32_e32 v88, v88
	v_mfma_f32_16x16x32_bf16 v[68:71], v[160:163], v[112:115], 0
	v_exp_f32_e32 v92, v92
	ds_read_b128 v[160:163], v201 offset:20480
	s_add_u32 s16, s22, s10
	s_addc_u32 s17, s23, s11
	s_add_u32 s15, s22, s12
	s_addc_u32 s14, s23, s13
	s_add_u32 s8, s16, 0x3bc00200
	s_addc_u32 s9, s17, 0
	s_add_u32 s6, s15, 0x23a50000
	s_addc_u32 s7, s14, 0
	v_mfma_f32_16x16x32_bf16 v[0:3], v[164:167], v[216:219], v[0:3]
	v_cvt_pk_bf16_f32 v242, v80, v81
	v_mfma_f32_16x16x32_bf16 v[4:7], v[164:167], v[238:241], v[4:7]
	v_exp_f32_e32 v89, v89
	ds_read_b128 v[164:167], v209 offset:8192
	s_waitcnt vmcnt(4)
	ds_write_b128 v225, v[152:155] offset:49152
	s_waitcnt lgkmcnt(7)
	v_mfma_f32_16x16x32_bf16 v[68:71], v[168:171], v[116:119], v[68:71]
	v_exp_f32_e32 v93, v93
	v_mfma_f32_16x16x32_bf16 v[64:67], v[168:171], v[100:103], v[64:67]
	v_cvt_pk_bf16_f32 v243, v82, v83
	ds_read_b128 v[168:171], v202 offset:20480
	ds_write_b128 v226, v[156:159] offset:49152
	v_mfma_f32_16x16x32_bf16 v[12:15], v[172:175], v[238:241], v[12:15]
	v_exp_f32_e32 v90, v90
	v_mfma_f32_16x16x32_bf16 v[8:11], v[172:175], v[216:219], v[8:11]
	v_exp_f32_e32 v94, v94
	ds_read_b128 v[172:175], v209 offset:10240
	ds_write_b64 v227, v[132:133] offset:32768
	s_waitcnt lgkmcnt(9)
	v_mfma_f32_16x16x32_bf16 v[64:67], v[176:179], v[104:107], v[64:67]
	v_cvt_pk_bf16_f32 v204, v84, v85
	v_mfma_f32_16x16x32_bf16 v[68:71], v[176:179], v[120:123], v[68:71]
	v_exp_f32_e32 v91, v91
	ds_read_b128 v[176:179], v203 offset:20480
	ds_write_b64 v228, v[134:135] offset:32768
	v_mfma_f32_16x16x32_bf16 v[16:19], v[180:183], v[216:219], v[16:19]
	v_exp_f32_e32 v95, v95
	v_mfma_f32_16x16x32_bf16 v[20:23], v[180:183], v[238:241], v[20:23]
	v_cvt_pk_bf16_f32 v205, v86, v87
	v_add_f32_e32 v220, v220, v88
	ds_read_b128 v[180:183], v209 offset:12288
	ds_write_b64 v229, v[128:129] offset:32768
	s_waitcnt lgkmcnt(11)
	v_mfma_f32_16x16x32_bf16 v[68:71], v[230:233], v[124:127], v[68:71]
	v_add_f32_e32 v221, v221, v92
	v_add_f32_e32 v220, v220, v89
	v_mfma_f32_16x16x32_bf16 v[64:67], v[230:233], v[108:111], v[64:67]
	v_add_f32_e32 v221, v221, v93
	v_cvt_pk_bf16_f32 v244, v88, v89
	ds_read_b128 v[230:233], v246 offset:20480
	ds_write_b64 v184, v[130:131] offset:32768
	v_mfma_f32_16x16x32_bf16 v[28:31], v[234:237], v[238:241], v[28:31]
	v_cvt_pk_bf16_f32 v245, v90, v91
	v_cvt_pk_bf16_f32 v206, v92, v93
	v_mfma_f32_16x16x32_bf16 v[24:27], v[234:237], v[216:219], v[24:27]
	v_cvt_pk_bf16_f32 v207, v94, v95
	ds_read_b128 v[234:237], v209 offset:14336
	global_load_dwordx4 v[132:135], v198, s[8:9]
	s_waitcnt lgkmcnt(12)
	v_mfma_f32_16x16x32_bf16 v[72:75], v[160:163], v[96:99], 0
	v_add_f32_e32 v220, v220, v90
	v_add_f32_e32 v221, v221, v94
	v_mfma_f32_16x16x32_bf16 v[76:79], v[160:163], v[112:115], 0
	v_add_f32_e32 v220, v220, v91
	v_add_f32_e32 v221, v221, v95
	ds_read_b128 v[160:163], v201 offset:24576
	global_load_dwordx4 v[128:131], v199, s[8:9]
	v_mfma_f32_16x16x32_bf16 v[32:35], v[164:167], v[216:219], v[32:35]
	v_add_f32_e32 v194, v194, v220
	v_add_f32_e32 v195, v195, v221
	v_mfma_f32_16x16x32_bf16 v[36:39], v[164:167], v[238:241], v[36:39]
	v_exp_f32_e32 v64, v64
	ds_read_b128 v[164:167], v210 offset:0
	global_load_dwordx4 v[152:155], v196, s[6:7]
	s_waitcnt lgkmcnt(10)
	v_mfma_f32_16x16x32_bf16 v[76:79], v[168:171], v[116:119], v[76:79]
	v_exp_f32_e32 v68, v68
	v_mfma_f32_16x16x32_bf16 v[72:75], v[168:171], v[100:103], v[72:75]
	v_exp_f32_e32 v65, v65
	ds_read_b128 v[168:171], v202 offset:24576
	global_load_dwordx4 v[156:159], v197, s[6:7]
	v_mfma_f32_16x16x32_bf16 v[44:47], v[172:175], v[238:241], v[44:47]
	v_exp_f32_e32 v69, v69
	v_mfma_f32_16x16x32_bf16 v[40:43], v[172:175], v[216:219], v[40:43]
	v_exp_f32_e32 v66, v66
	ds_read_b128 v[172:175], v210 offset:2048
	s_waitcnt lgkmcnt(8)
	v_mfma_f32_16x16x32_bf16 v[72:75], v[176:179], v[104:107], v[72:75]
	v_exp_f32_e32 v70, v70
	v_mfma_f32_16x16x32_bf16 v[76:79], v[176:179], v[120:123], v[76:79]
	v_exp_f32_e32 v67, v67
	ds_read_b128 v[176:179], v203 offset:24576
	v_mfma_f32_16x16x32_bf16 v[48:51], v[180:183], v[216:219], v[48:51]
	v_exp_f32_e32 v71, v71
	v_mfma_f32_16x16x32_bf16 v[52:55], v[180:183], v[238:241], v[52:55]
	v_add_f32_e32 v220, v64, v65
	ds_read_b128 v[180:183], v210 offset:4096
	s_waitcnt lgkmcnt(6)
	v_mfma_f32_16x16x32_bf16 v[76:79], v[230:233], v[124:127], v[76:79]
	v_add_f32_e32 v221, v68, v69
	v_mfma_f32_16x16x32_bf16 v[72:75], v[230:233], v[108:111], v[72:75]
	v_add_f32_e32 v220, v220, v66
	ds_read_b128 v[230:233], v246 offset:24576
	v_mfma_f32_16x16x32_bf16 v[60:63], v[234:237], v[238:241], v[60:63]
	v_add_f32_e32 v221, v221, v70
	v_add_f32_e32 v220, v220, v67
	v_mfma_f32_16x16x32_bf16 v[56:59], v[234:237], v[216:219], v[56:59]
	v_add_f32_e32 v221, v221, v71
	ds_read_b128 v[234:237], v210 offset:6144
	s_waitcnt lgkmcnt(6)
	v_mfma_f32_16x16x32_bf16 v[80:83], v[160:163], v[96:99], 0
	v_exp_f32_e32 v72, v72
	v_mfma_f32_16x16x32_bf16 v[84:87], v[160:163], v[112:115], 0
	v_exp_f32_e32 v76, v76
	ds_read_b128 v[160:163], v201 offset:28672
	v_mfma_f32_16x16x32_bf16 v[0:3], v[164:167], v[242:245], v[0:3]
	v_exp_f32_e32 v73, v73
	v_mfma_f32_16x16x32_bf16 v[4:7], v[164:167], v[204:207], v[4:7]
	v_exp_f32_e32 v77, v77
	ds_read_b128 v[164:167], v210 offset:8192
	s_waitcnt lgkmcnt(6)
	v_mfma_f32_16x16x32_bf16 v[84:87], v[168:171], v[116:119], v[84:87]
	v_exp_f32_e32 v74, v74
	v_mfma_f32_16x16x32_bf16 v[80:83], v[168:171], v[100:103], v[80:83]
	v_exp_f32_e32 v78, v78
	ds_read_b128 v[168:171], v202 offset:28672
	v_mfma_f32_16x16x32_bf16 v[12:15], v[172:175], v[204:207], v[12:15]
	v_exp_f32_e32 v75, v75
	v_mfma_f32_16x16x32_bf16 v[8:11], v[172:175], v[242:245], v[8:11]
	v_exp_f32_e32 v79, v79
	ds_read_b128 v[172:175], v210 offset:10240
	s_waitcnt lgkmcnt(6)
	v_mfma_f32_16x16x32_bf16 v[80:83], v[176:179], v[104:107], v[80:83]
	v_add_f32_e32 v220, v220, v72
	v_add_f32_e32 v221, v221, v76
	v_mfma_f32_16x16x32_bf16 v[84:87], v[176:179], v[120:123], v[84:87]
	v_add_f32_e32 v220, v220, v73
	ds_read_b128 v[176:179], v203 offset:28672
	v_mfma_f32_16x16x32_bf16 v[16:19], v[180:183], v[242:245], v[16:19]
	v_add_f32_e32 v221, v221, v77
	v_add_f32_e32 v220, v220, v74
	v_mfma_f32_16x16x32_bf16 v[20:23], v[180:183], v[204:207], v[20:23]
	v_add_f32_e32 v221, v221, v78
	ds_read_b128 v[180:183], v210 offset:12288
	s_waitcnt lgkmcnt(6)
	v_mfma_f32_16x16x32_bf16 v[84:87], v[230:233], v[124:127], v[84:87]
	v_add_f32_e32 v220, v220, v75
	v_add_f32_e32 v221, v221, v79
	v_mfma_f32_16x16x32_bf16 v[80:83], v[230:233], v[108:111], v[80:83]
	v_cvt_pk_bf16_f32 v216, v64, v65
	ds_read_b128 v[230:233], v246 offset:28672
	v_mfma_f32_16x16x32_bf16 v[28:31], v[234:237], v[204:207], v[28:31]
	v_cvt_pk_bf16_f32 v217, v66, v67
	v_cvt_pk_bf16_f32 v238, v68, v69
	v_mfma_f32_16x16x32_bf16 v[24:27], v[234:237], v[242:245], v[24:27]
	v_cvt_pk_bf16_f32 v239, v70, v71
	ds_read_b128 v[234:237], v210 offset:14336
	s_waitcnt lgkmcnt(6)
	v_mfma_f32_16x16x32_bf16 v[88:91], v[160:163], v[96:99], 0
	v_exp_f32_e32 v80, v80
	v_mfma_f32_16x16x32_bf16 v[92:95], v[160:163], v[112:115], 0
	v_exp_f32_e32 v84, v84
	ds_read_b128 v[160:163], v201 offset:32768
	v_mfma_f32_16x16x32_bf16 v[32:35], v[164:167], v[242:245], v[32:35]
	v_exp_f32_e32 v81, v81
	v_mfma_f32_16x16x32_bf16 v[36:39], v[164:167], v[204:207], v[36:39]
	v_exp_f32_e32 v85, v85
	ds_read_b128 v[164:167], v209 offset:16384
	s_waitcnt lgkmcnt(6)
	v_mfma_f32_16x16x32_bf16 v[92:95], v[168:171], v[116:119], v[92:95]
	v_exp_f32_e32 v82, v82
	v_mfma_f32_16x16x32_bf16 v[88:91], v[168:171], v[100:103], v[88:91]
	v_exp_f32_e32 v86, v86
	ds_read_b128 v[168:171], v202 offset:32768
	v_mfma_f32_16x16x32_bf16 v[44:47], v[172:175], v[204:207], v[44:47]
	v_exp_f32_e32 v83, v83
	v_mfma_f32_16x16x32_bf16 v[40:43], v[172:175], v[242:245], v[40:43]
	v_exp_f32_e32 v87, v87
	ds_read_b128 v[172:175], v209 offset:18432
	s_waitcnt lgkmcnt(6)
	v_mfma_f32_16x16x32_bf16 v[88:91], v[176:179], v[104:107], v[88:91]
	v_add_f32_e32 v220, v220, v80
	v_add_f32_e32 v221, v221, v84
	v_mfma_f32_16x16x32_bf16 v[92:95], v[176:179], v[120:123], v[92:95]
	v_add_f32_e32 v220, v220, v81
	ds_read_b128 v[176:179], v203 offset:32768
	v_mfma_f32_16x16x32_bf16 v[48:51], v[180:183], v[242:245], v[48:51]
	v_add_f32_e32 v221, v221, v85
	v_add_f32_e32 v220, v220, v82
	v_mfma_f32_16x16x32_bf16 v[52:55], v[180:183], v[204:207], v[52:55]
	v_add_f32_e32 v221, v221, v86
	ds_read_b128 v[180:183], v209 offset:20480
	s_waitcnt lgkmcnt(6)
	v_mfma_f32_16x16x32_bf16 v[92:95], v[230:233], v[124:127], v[92:95]
	v_add_f32_e32 v220, v220, v83
	v_add_f32_e32 v221, v221, v87
	v_mfma_f32_16x16x32_bf16 v[88:91], v[230:233], v[108:111], v[88:91]
	v_cvt_pk_bf16_f32 v218, v72, v73
	ds_read_b128 v[230:233], v246 offset:32768
	v_mfma_f32_16x16x32_bf16 v[60:63], v[234:237], v[204:207], v[60:63]
	v_cvt_pk_bf16_f32 v219, v74, v75
	v_cvt_pk_bf16_f32 v240, v76, v77
	v_mfma_f32_16x16x32_bf16 v[56:59], v[234:237], v[242:245], v[56:59]
	v_cvt_pk_bf16_f32 v241, v78, v79
	ds_read_b128 v[234:237], v209 offset:22528
	s_cmp_eq_u32 s100, 1
	s_cbranch_scc1 .Lattn_pa1
	s_setprio 1
	s_branch .Lattn_pb1

.Lattn_pb1:
	s_waitcnt lgkmcnt(6)
	v_mfma_f32_16x16x32_bf16 v[64:67], v[160:163], v[96:99], 0
	v_exp_f32_e32 v88, v88
	v_mfma_f32_16x16x32_bf16 v[68:71], v[160:163], v[112:115], 0
	v_exp_f32_e32 v92, v92
	ds_read_b128 v[160:163], v201 offset:36864
	s_add_u32 s8, s16, 0x3bc00280
	s_addc_u32 s9, s17, 0
	s_add_u32 s6, s15, 0x23a60000
	s_addc_u32 s7, s14, 0
	v_mfma_f32_16x16x32_bf16 v[0:3], v[164:167], v[216:219], v[0:3]
	v_cvt_pk_bf16_f32 v242, v80, v81
	v_mfma_f32_16x16x32_bf16 v[4:7], v[164:167], v[238:241], v[4:7]
	v_exp_f32_e32 v89, v89
	ds_read_b128 v[164:167], v209 offset:24576
	s_waitcnt vmcnt(4)
	ds_write_b128 v225, v[136:139] offset:0
	s_waitcnt lgkmcnt(7)
	v_mfma_f32_16x16x32_bf16 v[68:71], v[168:171], v[116:119], v[68:71]
	v_exp_f32_e32 v93, v93
	v_mfma_f32_16x16x32_bf16 v[64:67], v[168:171], v[100:103], v[64:67]
	v_cvt_pk_bf16_f32 v243, v82, v83
	ds_read_b128 v[168:171], v202 offset:36864
	ds_write_b128 v226, v[140:143] offset:0
	v_mfma_f32_16x16x32_bf16 v[12:15], v[172:175], v[238:241], v[12:15]
	v_exp_f32_e32 v90, v90
	v_mfma_f32_16x16x32_bf16 v[8:11], v[172:175], v[216:219], v[8:11]
	v_exp_f32_e32 v94, v94
	ds_read_b128 v[172:175], v209 offset:26624
	ds_write_b64 v227, v[148:149] offset:49152
	s_waitcnt lgkmcnt(9)
	v_mfma_f32_16x16x32_bf16 v[64:67], v[176:179], v[104:107], v[64:67]
	v_cvt_pk_bf16_f32 v204, v84, v85
	v_mfma_f32_16x16x32_bf16 v[68:71], v[176:179], v[120:123], v[68:71]
	v_exp_f32_e32 v91, v91
	ds_read_b128 v[176:179], v203 offset:36864
	ds_write_b64 v228, v[150:151] offset:49152
	v_mfma_f32_16x16x32_bf16 v[16:19], v[180:183], v[216:219], v[16:19]
	v_exp_f32_e32 v95, v95
	v_mfma_f32_16x16x32_bf16 v[20:23], v[180:183], v[238:241], v[20:23]
	v_cvt_pk_bf16_f32 v205, v86, v87
	v_add_f32_e32 v220, v220, v88
	ds_read_b128 v[180:183], v209 offset:28672
	ds_write_b64 v229, v[144:145] offset:49152
	s_waitcnt lgkmcnt(11)
	v_mfma_f32_16x16x32_bf16 v[68:71], v[230:233], v[124:127], v[68:71]
	v_add_f32_e32 v221, v221, v92
	v_add_f32_e32 v220, v220, v89
	v_mfma_f32_16x16x32_bf16 v[64:67], v[230:233], v[108:111], v[64:67]
	v_add_f32_e32 v221, v221, v93
	v_cvt_pk_bf16_f32 v244, v88, v89
	ds_read_b128 v[230:233], v246 offset:36864
	ds_write_b64 v184, v[146:147] offset:49152
	v_mfma_f32_16x16x32_bf16 v[28:31], v[234:237], v[238:241], v[28:31]
	v_cvt_pk_bf16_f32 v245, v90, v91
	v_cvt_pk_bf16_f32 v206, v92, v93
	v_mfma_f32_16x16x32_bf16 v[24:27], v[234:237], v[216:219], v[24:27]
	v_cvt_pk_bf16_f32 v207, v94, v95
	ds_read_b128 v[234:237], v209 offset:30720
	global_load_dwordx4 v[148:151], v198, s[8:9]
	s_waitcnt lgkmcnt(12)
	v_mfma_f32_16x16x32_bf16 v[72:75], v[160:163], v[96:99], 0
	v_add_f32_e32 v220, v220, v90
	v_add_f32_e32 v221, v221, v94
	v_mfma_f32_16x16x32_bf16 v[76:79], v[160:163], v[112:115], 0
	v_add_f32_e32 v220, v220, v91
	v_add_f32_e32 v221, v221, v95
	ds_read_b128 v[160:163], v201 offset:40960
	global_load_dwordx4 v[144:147], v199, s[8:9]
	v_mfma_f32_16x16x32_bf16 v[32:35], v[164:167], v[216:219], v[32:35]
	v_add_f32_e32 v194, v194, v220
	v_add_f32_e32 v195, v195, v221
	v_mfma_f32_16x16x32_bf16 v[36:39], v[164:167], v[238:241], v[36:39]
	v_exp_f32_e32 v64, v64
	ds_read_b128 v[164:167], v210 offset:16384
	global_load_dwordx4 v[136:139], v196, s[6:7]
	s_waitcnt lgkmcnt(10)
	v_mfma_f32_16x16x32_bf16 v[76:79], v[168:171], v[116:119], v[76:79]
	v_exp_f32_e32 v68, v68
	v_mfma_f32_16x16x32_bf16 v[72:75], v[168:171], v[100:103], v[72:75]
	v_exp_f32_e32 v65, v65
	ds_read_b128 v[168:171], v202 offset:40960
	global_load_dwordx4 v[140:143], v197, s[6:7]
	v_mfma_f32_16x16x32_bf16 v[44:47], v[172:175], v[238:241], v[44:47]
	v_exp_f32_e32 v69, v69
	v_mfma_f32_16x16x32_bf16 v[40:43], v[172:175], v[216:219], v[40:43]
	v_exp_f32_e32 v66, v66
	ds_read_b128 v[172:175], v210 offset:18432
	s_waitcnt lgkmcnt(8)
	v_mfma_f32_16x16x32_bf16 v[72:75], v[176:179], v[104:107], v[72:75]
	v_exp_f32_e32 v70, v70
	v_mfma_f32_16x16x32_bf16 v[76:79], v[176:179], v[120:123], v[76:79]
	v_exp_f32_e32 v67, v67
	ds_read_b128 v[176:179], v203 offset:40960
	v_mfma_f32_16x16x32_bf16 v[48:51], v[180:183], v[216:219], v[48:51]
	v_exp_f32_e32 v71, v71
	v_mfma_f32_16x16x32_bf16 v[52:55], v[180:183], v[238:241], v[52:55]
	v_add_f32_e32 v220, v64, v65
	ds_read_b128 v[180:183], v210 offset:20480
	s_waitcnt lgkmcnt(6)
	v_mfma_f32_16x16x32_bf16 v[76:79], v[230:233], v[124:127], v[76:79]
	v_add_f32_e32 v221, v68, v69
	v_mfma_f32_16x16x32_bf16 v[72:75], v[230:233], v[108:111], v[72:75]
	v_add_f32_e32 v220, v220, v66
	ds_read_b128 v[230:233], v246 offset:40960
	v_mfma_f32_16x16x32_bf16 v[60:63], v[234:237], v[238:241], v[60:63]
	v_add_f32_e32 v221, v221, v70
	v_add_f32_e32 v220, v220, v67
	v_mfma_f32_16x16x32_bf16 v[56:59], v[234:237], v[216:219], v[56:59]
	v_add_f32_e32 v221, v221, v71
	ds_read_b128 v[234:237], v210 offset:22528
	s_waitcnt lgkmcnt(6)
	v_mfma_f32_16x16x32_bf16 v[80:83], v[160:163], v[96:99], 0
	v_exp_f32_e32 v72, v72
	v_mfma_f32_16x16x32_bf16 v[84:87], v[160:163], v[112:115], 0
	v_exp_f32_e32 v76, v76
	ds_read_b128 v[160:163], v201 offset:45056
	v_mfma_f32_16x16x32_bf16 v[0:3], v[164:167], v[242:245], v[0:3]
	v_exp_f32_e32 v73, v73
	v_mfma_f32_16x16x32_bf16 v[4:7], v[164:167], v[204:207], v[4:7]
	v_exp_f32_e32 v77, v77
	ds_read_b128 v[164:167], v210 offset:24576
	s_waitcnt lgkmcnt(6)
	v_mfma_f32_16x16x32_bf16 v[84:87], v[168:171], v[116:119], v[84:87]
	v_exp_f32_e32 v74, v74
	v_mfma_f32_16x16x32_bf16 v[80:83], v[168:171], v[100:103], v[80:83]
	v_exp_f32_e32 v78, v78
	ds_read_b128 v[168:171], v202 offset:45056
	v_mfma_f32_16x16x32_bf16 v[12:15], v[172:175], v[204:207], v[12:15]
	v_exp_f32_e32 v75, v75
	v_mfma_f32_16x16x32_bf16 v[8:11], v[172:175], v[242:245], v[8:11]
	v_exp_f32_e32 v79, v79
	ds_read_b128 v[172:175], v210 offset:26624
	s_waitcnt lgkmcnt(6)
	v_mfma_f32_16x16x32_bf16 v[80:83], v[176:179], v[104:107], v[80:83]
	v_add_f32_e32 v220, v220, v72
	v_add_f32_e32 v221, v221, v76
	v_mfma_f32_16x16x32_bf16 v[84:87], v[176:179], v[120:123], v[84:87]
	v_add_f32_e32 v220, v220, v73
	ds_read_b128 v[176:179], v203 offset:45056
	v_mfma_f32_16x16x32_bf16 v[16:19], v[180:183], v[242:245], v[16:19]
	v_add_f32_e32 v221, v221, v77
	v_add_f32_e32 v220, v220, v74
	v_mfma_f32_16x16x32_bf16 v[20:23], v[180:183], v[204:207], v[20:23]
	v_add_f32_e32 v221, v221, v78
	ds_read_b128 v[180:183], v210 offset:28672
	s_waitcnt lgkmcnt(6)
	v_mfma_f32_16x16x32_bf16 v[84:87], v[230:233], v[124:127], v[84:87]
	v_add_f32_e32 v220, v220, v75
	v_add_f32_e32 v221, v221, v79
	v_mfma_f32_16x16x32_bf16 v[80:83], v[230:233], v[108:111], v[80:83]
	v_cvt_pk_bf16_f32 v216, v64, v65
	ds_read_b128 v[230:233], v246 offset:45056
	v_mfma_f32_16x16x32_bf16 v[28:31], v[234:237], v[204:207], v[28:31]
	v_cvt_pk_bf16_f32 v217, v66, v67
	v_cvt_pk_bf16_f32 v238, v68, v69
	v_mfma_f32_16x16x32_bf16 v[24:27], v[234:237], v[242:245], v[24:27]
	v_cvt_pk_bf16_f32 v239, v70, v71
	ds_read_b128 v[234:237], v210 offset:30720
	s_waitcnt lgkmcnt(6)
	v_mfma_f32_16x16x32_bf16 v[88:91], v[160:163], v[96:99], 0
	v_exp_f32_e32 v80, v80
	v_mfma_f32_16x16x32_bf16 v[92:95], v[160:163], v[112:115], 0
	v_exp_f32_e32 v84, v84
	v_mfma_f32_16x16x32_bf16 v[32:35], v[164:167], v[242:245], v[32:35]
	v_exp_f32_e32 v81, v81
	v_mfma_f32_16x16x32_bf16 v[36:39], v[164:167], v[204:207], v[36:39]
	v_exp_f32_e32 v85, v85
	s_waitcnt lgkmcnt(4)
	v_mfma_f32_16x16x32_bf16 v[92:95], v[168:171], v[116:119], v[92:95]
	v_exp_f32_e32 v82, v82
	v_mfma_f32_16x16x32_bf16 v[88:91], v[168:171], v[100:103], v[88:91]
	v_exp_f32_e32 v86, v86
	v_mfma_f32_16x16x32_bf16 v[44:47], v[172:175], v[204:207], v[44:47]
	v_exp_f32_e32 v83, v83
	v_mfma_f32_16x16x32_bf16 v[40:43], v[172:175], v[242:245], v[40:43]
	v_exp_f32_e32 v87, v87
	s_waitcnt lgkmcnt(3)
	v_mfma_f32_16x16x32_bf16 v[88:91], v[176:179], v[104:107], v[88:91]
	v_add_f32_e32 v220, v220, v80
	v_add_f32_e32 v221, v221, v84
	v_mfma_f32_16x16x32_bf16 v[92:95], v[176:179], v[120:123], v[92:95]
	v_add_f32_e32 v220, v220, v81
	s_waitcnt lgkmcnt(0)
	s_barrier
	ds_read_b128 v[160:163], v201 offset:49152
	ds_read_b128 v[164:167], v209 offset:32768
	ds_read_b128 v[168:171], v202 offset:49152
	ds_read_b128 v[172:175], v209 offset:34816
	ds_read_b128 v[176:179], v203 offset:49152
	v_mfma_f32_16x16x32_bf16 v[48:51], v[180:183], v[242:245], v[48:51]
	v_add_f32_e32 v221, v221, v85
	v_add_f32_e32 v220, v220, v82
	v_mfma_f32_16x16x32_bf16 v[52:55], v[180:183], v[204:207], v[52:55]
	v_add_f32_e32 v221, v221, v86
	ds_read_b128 v[180:183], v209 offset:36864
	v_mfma_f32_16x16x32_bf16 v[92:95], v[230:233], v[124:127], v[92:95]
	v_add_f32_e32 v220, v220, v83
	v_add_f32_e32 v221, v221, v87
	v_mfma_f32_16x16x32_bf16 v[88:91], v[230:233], v[108:111], v[88:91]
	v_cvt_pk_bf16_f32 v218, v72, v73
	ds_read_b128 v[230:233], v246 offset:49152
	v_mfma_f32_16x16x32_bf16 v[60:63], v[234:237], v[204:207], v[60:63]
	v_cvt_pk_bf16_f32 v219, v74, v75
	v_cvt_pk_bf16_f32 v240, v76, v77
	v_mfma_f32_16x16x32_bf16 v[56:59], v[234:237], v[242:245], v[56:59]
	v_cvt_pk_bf16_f32 v241, v78, v79
	ds_read_b128 v[234:237], v209 offset:38912
	s_cmp_eq_u32 s100, 0
	s_cbranch_scc1 .Lattn_pa2
	s_setprio 1
	s_branch .Lattn_pb2

.Lattn_pb2:
	s_waitcnt lgkmcnt(6)
	v_mfma_f32_16x16x32_bf16 v[64:67], v[160:163], v[96:99], 0
	v_exp_f32_e32 v88, v88
	v_mfma_f32_16x16x32_bf16 v[68:71], v[160:163], v[112:115], 0
	v_exp_f32_e32 v92, v92
	ds_read_b128 v[160:163], v201 offset:53248
	s_add_u32 s8, s16, 0x3bc00300
	s_addc_u32 s9, s17, 0
	s_add_u32 s6, s15, 0x23a70000
	s_addc_u32 s7, s14, 0
	v_mfma_f32_16x16x32_bf16 v[0:3], v[164:167], v[216:219], v[0:3]
	v_cvt_pk_bf16_f32 v242, v80, v81
	v_mfma_f32_16x16x32_bf16 v[4:7], v[164:167], v[238:241], v[4:7]
	v_exp_f32_e32 v89, v89
	ds_read_b128 v[164:167], v209 offset:40960
	s_waitcnt vmcnt(4)
	ds_write_b128 v225, v[152:155] offset:16384
	s_waitcnt lgkmcnt(7)
	v_mfma_f32_16x16x32_bf16 v[68:71], v[168:171], v[116:119], v[68:71]
	v_exp_f32_e32 v93, v93
	v_mfma_f32_16x16x32_bf16 v[64:67], v[168:171], v[100:103], v[64:67]
	v_cvt_pk_bf16_f32 v243, v82, v83
	ds_read_b128 v[168:171], v202 offset:53248
	ds_write_b128 v226, v[156:159] offset:16384
	v_mfma_f32_16x16x32_bf16 v[12:15], v[172:175], v[238:241], v[12:15]
	v_exp_f32_e32 v90, v90
	v_mfma_f32_16x16x32_bf16 v[8:11], v[172:175], v[216:219], v[8:11]
	v_exp_f32_e32 v94, v94
	ds_read_b128 v[172:175], v209 offset:43008
	ds_write_b64 v227, v[132:133] offset:0
	s_waitcnt lgkmcnt(9)
	v_mfma_f32_16x16x32_bf16 v[64:67], v[176:179], v[104:107], v[64:67]
	v_cvt_pk_bf16_f32 v204, v84, v85
	v_mfma_f32_16x16x32_bf16 v[68:71], v[176:179], v[120:123], v[68:71]
	v_exp_f32_e32 v91, v91
	ds_read_b128 v[176:179], v203 offset:53248
	ds_write_b64 v228, v[134:135] offset:0
	v_mfma_f32_16x16x32_bf16 v[16:19], v[180:183], v[216:219], v[16:19]
	v_exp_f32_e32 v95, v95
	v_mfma_f32_16x16x32_bf16 v[20:23], v[180:183], v[238:241], v[20:23]
	v_cvt_pk_bf16_f32 v205, v86, v87
	v_add_f32_e32 v220, v220, v88
	ds_read_b128 v[180:183], v209 offset:45056
	ds_write_b64 v229, v[128:129] offset:0
	s_waitcnt lgkmcnt(11)
	v_mfma_f32_16x16x32_bf16 v[68:71], v[230:233], v[124:127], v[68:71]
	v_add_f32_e32 v221, v221, v92
	v_add_f32_e32 v220, v220, v89
	v_mfma_f32_16x16x32_bf16 v[64:67], v[230:233], v[108:111], v[64:67]
	v_add_f32_e32 v221, v221, v93
	v_cvt_pk_bf16_f32 v244, v88, v89
	ds_read_b128 v[230:233], v246 offset:53248
	ds_write_b64 v184, v[130:131] offset:0
	v_mfma_f32_16x16x32_bf16 v[28:31], v[234:237], v[238:241], v[28:31]
	v_cvt_pk_bf16_f32 v245, v90, v91
	v_cvt_pk_bf16_f32 v206, v92, v93
	v_mfma_f32_16x16x32_bf16 v[24:27], v[234:237], v[216:219], v[24:27]
	v_cvt_pk_bf16_f32 v207, v94, v95
	ds_read_b128 v[234:237], v209 offset:47104
	global_load_dwordx4 v[132:135], v198, s[8:9]
	s_waitcnt lgkmcnt(12)
	v_mfma_f32_16x16x32_bf16 v[72:75], v[160:163], v[96:99], 0
	v_add_f32_e32 v220, v220, v90
	v_add_f32_e32 v221, v221, v94
	v_mfma_f32_16x16x32_bf16 v[76:79], v[160:163], v[112:115], 0
	v_add_f32_e32 v220, v220, v91
	v_add_f32_e32 v221, v221, v95
	ds_read_b128 v[160:163], v201 offset:57344
	global_load_dwordx4 v[128:131], v199, s[8:9]
	v_mfma_f32_16x16x32_bf16 v[32:35], v[164:167], v[216:219], v[32:35]
	v_add_f32_e32 v194, v194, v220
	v_add_f32_e32 v195, v195, v221
	v_mfma_f32_16x16x32_bf16 v[36:39], v[164:167], v[238:241], v[36:39]
	v_exp_f32_e32 v64, v64
	ds_read_b128 v[164:167], v210 offset:32768
	global_load_dwordx4 v[152:155], v196, s[6:7]
	s_waitcnt lgkmcnt(10)
	v_mfma_f32_16x16x32_bf16 v[76:79], v[168:171], v[116:119], v[76:79]
	v_exp_f32_e32 v68, v68
	v_mfma_f32_16x16x32_bf16 v[72:75], v[168:171], v[100:103], v[72:75]
	v_exp_f32_e32 v65, v65
	ds_read_b128 v[168:171], v202 offset:57344
	global_load_dwordx4 v[156:159], v197, s[6:7]
	v_mfma_f32_16x16x32_bf16 v[44:47], v[172:175], v[238:241], v[44:47]
	v_exp_f32_e32 v69, v69
	v_mfma_f32_16x16x32_bf16 v[40:43], v[172:175], v[216:219], v[40:43]
	v_exp_f32_e32 v66, v66
	ds_read_b128 v[172:175], v210 offset:34816
	s_waitcnt lgkmcnt(8)
	v_mfma_f32_16x16x32_bf16 v[72:75], v[176:179], v[104:107], v[72:75]
	v_exp_f32_e32 v70, v70
	v_mfma_f32_16x16x32_bf16 v[76:79], v[176:179], v[120:123], v[76:79]
	v_exp_f32_e32 v67, v67
	ds_read_b128 v[176:179], v203 offset:57344
	v_mfma_f32_16x16x32_bf16 v[48:51], v[180:183], v[216:219], v[48:51]
	v_exp_f32_e32 v71, v71
	v_mfma_f32_16x16x32_bf16 v[52:55], v[180:183], v[238:241], v[52:55]
	v_add_f32_e32 v220, v64, v65
	ds_read_b128 v[180:183], v210 offset:36864
	s_waitcnt lgkmcnt(6)
	v_mfma_f32_16x16x32_bf16 v[76:79], v[230:233], v[124:127], v[76:79]
	v_add_f32_e32 v221, v68, v69
	v_mfma_f32_16x16x32_bf16 v[72:75], v[230:233], v[108:111], v[72:75]
	v_add_f32_e32 v220, v220, v66
	ds_read_b128 v[230:233], v246 offset:57344
	v_mfma_f32_16x16x32_bf16 v[60:63], v[234:237], v[238:241], v[60:63]
	v_add_f32_e32 v221, v221, v70
	v_add_f32_e32 v220, v220, v67
	v_mfma_f32_16x16x32_bf16 v[56:59], v[234:237], v[216:219], v[56:59]
	v_add_f32_e32 v221, v221, v71
	ds_read_b128 v[234:237], v210 offset:38912
	s_waitcnt lgkmcnt(6)
	v_mfma_f32_16x16x32_bf16 v[80:83], v[160:163], v[96:99], 0
	v_exp_f32_e32 v72, v72
	v_mfma_f32_16x16x32_bf16 v[84:87], v[160:163], v[112:115], 0
	v_exp_f32_e32 v76, v76
	ds_read_b128 v[160:163], v201 offset:61440
	v_mfma_f32_16x16x32_bf16 v[0:3], v[164:167], v[242:245], v[0:3]
	v_exp_f32_e32 v73, v73
	v_mfma_f32_16x16x32_bf16 v[4:7], v[164:167], v[204:207], v[4:7]
	v_exp_f32_e32 v77, v77
	ds_read_b128 v[164:167], v210 offset:40960
	s_waitcnt lgkmcnt(6)
	v_mfma_f32_16x16x32_bf16 v[84:87], v[168:171], v[116:119], v[84:87]
	v_exp_f32_e32 v74, v74
	v_mfma_f32_16x16x32_bf16 v[80:83], v[168:171], v[100:103], v[80:83]
	v_exp_f32_e32 v78, v78
	ds_read_b128 v[168:171], v202 offset:61440
	v_mfma_f32_16x16x32_bf16 v[12:15], v[172:175], v[204:207], v[12:15]
	v_exp_f32_e32 v75, v75
	v_mfma_f32_16x16x32_bf16 v[8:11], v[172:175], v[242:245], v[8:11]
	v_exp_f32_e32 v79, v79
	ds_read_b128 v[172:175], v210 offset:43008
	s_waitcnt lgkmcnt(6)
	v_mfma_f32_16x16x32_bf16 v[80:83], v[176:179], v[104:107], v[80:83]
	v_add_f32_e32 v220, v220, v72
	v_add_f32_e32 v221, v221, v76
	v_mfma_f32_16x16x32_bf16 v[84:87], v[176:179], v[120:123], v[84:87]
	v_add_f32_e32 v220, v220, v73
	ds_read_b128 v[176:179], v203 offset:61440
	v_mfma_f32_16x16x32_bf16 v[16:19], v[180:183], v[242:245], v[16:19]
	v_add_f32_e32 v221, v221, v77
	v_add_f32_e32 v220, v220, v74
	v_mfma_f32_16x16x32_bf16 v[20:23], v[180:183], v[204:207], v[20:23]
	v_add_f32_e32 v221, v221, v78
	ds_read_b128 v[180:183], v210 offset:45056
	s_waitcnt lgkmcnt(6)
	v_mfma_f32_16x16x32_bf16 v[84:87], v[230:233], v[124:127], v[84:87]
	v_add_f32_e32 v220, v220, v75
	v_add_f32_e32 v221, v221, v79
	v_mfma_f32_16x16x32_bf16 v[80:83], v[230:233], v[108:111], v[80:83]
	v_cvt_pk_bf16_f32 v216, v64, v65
	ds_read_b128 v[230:233], v246 offset:61440
	v_mfma_f32_16x16x32_bf16 v[28:31], v[234:237], v[204:207], v[28:31]
	v_cvt_pk_bf16_f32 v217, v66, v67
	v_cvt_pk_bf16_f32 v238, v68, v69
	v_mfma_f32_16x16x32_bf16 v[24:27], v[234:237], v[242:245], v[24:27]
	v_cvt_pk_bf16_f32 v239, v70, v71
	ds_read_b128 v[234:237], v210 offset:47104
	s_waitcnt lgkmcnt(6)
	v_mfma_f32_16x16x32_bf16 v[88:91], v[160:163], v[96:99], 0
	v_exp_f32_e32 v80, v80
	v_mfma_f32_16x16x32_bf16 v[92:95], v[160:163], v[112:115], 0
	v_exp_f32_e32 v84, v84
	ds_read_b128 v[160:163], v201 offset:0
	v_mfma_f32_16x16x32_bf16 v[32:35], v[164:167], v[242:245], v[32:35]
	v_exp_f32_e32 v81, v81
	v_mfma_f32_16x16x32_bf16 v[36:39], v[164:167], v[204:207], v[36:39]
	v_exp_f32_e32 v85, v85
	ds_read_b128 v[164:167], v209 offset:49152
	s_waitcnt lgkmcnt(6)
	v_mfma_f32_16x16x32_bf16 v[92:95], v[168:171], v[116:119], v[92:95]
	v_exp_f32_e32 v82, v82
	v_mfma_f32_16x16x32_bf16 v[88:91], v[168:171], v[100:103], v[88:91]
	v_exp_f32_e32 v86, v86
	ds_read_b128 v[168:171], v202 offset:0
	v_mfma_f32_16x16x32_bf16 v[44:47], v[172:175], v[204:207], v[44:47]
	v_exp_f32_e32 v83, v83
	v_mfma_f32_16x16x32_bf16 v[40:43], v[172:175], v[242:245], v[40:43]
	v_exp_f32_e32 v87, v87
	ds_read_b128 v[172:175], v209 offset:51200
	s_waitcnt lgkmcnt(6)
	v_mfma_f32_16x16x32_bf16 v[88:91], v[176:179], v[104:107], v[88:91]
	v_add_f32_e32 v220, v220, v80
	v_add_f32_e32 v221, v221, v84
	v_mfma_f32_16x16x32_bf16 v[92:95], v[176:179], v[120:123], v[92:95]
	v_add_f32_e32 v220, v220, v81
	ds_read_b128 v[176:179], v203 offset:0
	v_mfma_f32_16x16x32_bf16 v[48:51], v[180:183], v[242:245], v[48:51]
	v_add_f32_e32 v221, v221, v85
	v_add_f32_e32 v220, v220, v82
	v_mfma_f32_16x16x32_bf16 v[52:55], v[180:183], v[204:207], v[52:55]
	v_add_f32_e32 v221, v221, v86
	ds_read_b128 v[180:183], v209 offset:53248
	s_waitcnt lgkmcnt(6)
	v_mfma_f32_16x16x32_bf16 v[92:95], v[230:233], v[124:127], v[92:95]
	v_add_f32_e32 v220, v220, v83
	v_add_f32_e32 v221, v221, v87
	v_mfma_f32_16x16x32_bf16 v[88:91], v[230:233], v[108:111], v[88:91]
	v_cvt_pk_bf16_f32 v218, v72, v73
	ds_read_b128 v[230:233], v246 offset:0
	v_mfma_f32_16x16x32_bf16 v[60:63], v[234:237], v[204:207], v[60:63]
	v_cvt_pk_bf16_f32 v219, v74, v75
	v_cvt_pk_bf16_f32 v240, v76, v77
	v_mfma_f32_16x16x32_bf16 v[56:59], v[234:237], v[242:245], v[56:59]
	v_cvt_pk_bf16_f32 v241, v78, v79
	ds_read_b128 v[234:237], v209 offset:55296
	s_cmp_eq_u32 s100, 1
	s_cbranch_scc1 .Lattn_pa3
	s_setprio 1
	s_branch .Lattn_pb3

.Lattn_pb3:
	s_waitcnt lgkmcnt(6)
	v_mfma_f32_16x16x32_bf16 v[64:67], v[160:163], v[96:99], 0
	v_exp_f32_e32 v88, v88
	v_mfma_f32_16x16x32_bf16 v[68:71], v[160:163], v[112:115], 0
	v_exp_f32_e32 v92, v92
	ds_read_b128 v[160:163], v201 offset:4096
	s_add_u32 s8, s16, 0x3bc00380
	s_addc_u32 s9, s17, 0
	s_add_u32 s6, s15, 0x23a80000
	s_addc_u32 s7, s14, 0
	v_mfma_f32_16x16x32_bf16 v[0:3], v[164:167], v[216:219], v[0:3]
	v_cvt_pk_bf16_f32 v242, v80, v81
	v_mfma_f32_16x16x32_bf16 v[4:7], v[164:167], v[238:241], v[4:7]
	v_exp_f32_e32 v89, v89
	ds_read_b128 v[164:167], v209 offset:57344
	s_waitcnt vmcnt(4)
	ds_write_b128 v225, v[136:139] offset:32768
	s_waitcnt lgkmcnt(7)
	v_mfma_f32_16x16x32_bf16 v[68:71], v[168:171], v[116:119], v[68:71]
	v_exp_f32_e32 v93, v93
	v_mfma_f32_16x16x32_bf16 v[64:67], v[168:171], v[100:103], v[64:67]
	v_cvt_pk_bf16_f32 v243, v82, v83
	ds_read_b128 v[168:171], v202 offset:4096
	ds_write_b128 v226, v[140:143] offset:32768
	v_mfma_f32_16x16x32_bf16 v[12:15], v[172:175], v[238:241], v[12:15]
	v_exp_f32_e32 v90, v90
	v_mfma_f32_16x16x32_bf16 v[8:11], v[172:175], v[216:219], v[8:11]
	v_exp_f32_e32 v94, v94
	ds_read_b128 v[172:175], v209 offset:59392
	ds_write_b64 v227, v[148:149] offset:16384
	s_waitcnt lgkmcnt(9)
	v_mfma_f32_16x16x32_bf16 v[64:67], v[176:179], v[104:107], v[64:67]
	v_cvt_pk_bf16_f32 v204, v84, v85
	v_mfma_f32_16x16x32_bf16 v[68:71], v[176:179], v[120:123], v[68:71]
	v_exp_f32_e32 v91, v91
	ds_read_b128 v[176:179], v203 offset:4096
	ds_write_b64 v228, v[150:151] offset:16384
	v_mfma_f32_16x16x32_bf16 v[16:19], v[180:183], v[216:219], v[16:19]
	v_exp_f32_e32 v95, v95
	v_mfma_f32_16x16x32_bf16 v[20:23], v[180:183], v[238:241], v[20:23]
	v_cvt_pk_bf16_f32 v205, v86, v87
	v_add_f32_e32 v220, v220, v88
	ds_read_b128 v[180:183], v209 offset:61440
	ds_write_b64 v229, v[144:145] offset:16384
	s_waitcnt lgkmcnt(11)
	v_mfma_f32_16x16x32_bf16 v[68:71], v[230:233], v[124:127], v[68:71]
	v_add_f32_e32 v221, v221, v92
	v_add_f32_e32 v220, v220, v89
	v_mfma_f32_16x16x32_bf16 v[64:67], v[230:233], v[108:111], v[64:67]
	v_add_f32_e32 v221, v221, v93
	v_cvt_pk_bf16_f32 v244, v88, v89
	ds_read_b128 v[230:233], v246 offset:4096
	ds_write_b64 v184, v[146:147] offset:16384
	v_mfma_f32_16x16x32_bf16 v[28:31], v[234:237], v[238:241], v[28:31]
	v_cvt_pk_bf16_f32 v245, v90, v91
	v_cvt_pk_bf16_f32 v206, v92, v93
	v_mfma_f32_16x16x32_bf16 v[24:27], v[234:237], v[216:219], v[24:27]
	v_cvt_pk_bf16_f32 v207, v94, v95
	ds_read_b128 v[234:237], v209 offset:63488
	global_load_dwordx4 v[148:151], v198, s[8:9]
	s_waitcnt lgkmcnt(12)
	v_mfma_f32_16x16x32_bf16 v[72:75], v[160:163], v[96:99], 0
	v_add_f32_e32 v220, v220, v90
	v_add_f32_e32 v221, v221, v94
	v_mfma_f32_16x16x32_bf16 v[76:79], v[160:163], v[112:115], 0
	v_add_f32_e32 v220, v220, v91
	v_add_f32_e32 v221, v221, v95
	ds_read_b128 v[160:163], v201 offset:8192
	global_load_dwordx4 v[144:147], v199, s[8:9]
	v_mfma_f32_16x16x32_bf16 v[32:35], v[164:167], v[216:219], v[32:35]
	v_add_f32_e32 v194, v194, v220
	v_add_f32_e32 v195, v195, v221
	v_mfma_f32_16x16x32_bf16 v[36:39], v[164:167], v[238:241], v[36:39]
	v_exp_f32_e32 v64, v64
	ds_read_b128 v[164:167], v210 offset:49152
	global_load_dwordx4 v[136:139], v196, s[6:7]
	s_waitcnt lgkmcnt(10)
	v_mfma_f32_16x16x32_bf16 v[76:79], v[168:171], v[116:119], v[76:79]
	v_exp_f32_e32 v68, v68
	v_mfma_f32_16x16x32_bf16 v[72:75], v[168:171], v[100:103], v[72:75]
	v_exp_f32_e32 v65, v65
	ds_read_b128 v[168:171], v202 offset:8192
	global_load_dwordx4 v[140:143], v197, s[6:7]
	v_mfma_f32_16x16x32_bf16 v[44:47], v[172:175], v[238:241], v[44:47]
	v_exp_f32_e32 v69, v69
	v_mfma_f32_16x16x32_bf16 v[40:43], v[172:175], v[216:219], v[40:43]
	v_exp_f32_e32 v66, v66
	ds_read_b128 v[172:175], v210 offset:51200
	s_waitcnt lgkmcnt(8)
	v_mfma_f32_16x16x32_bf16 v[72:75], v[176:179], v[104:107], v[72:75]
	v_exp_f32_e32 v70, v70
	v_mfma_f32_16x16x32_bf16 v[76:79], v[176:179], v[120:123], v[76:79]
	v_exp_f32_e32 v67, v67
	ds_read_b128 v[176:179], v203 offset:8192
	v_mfma_f32_16x16x32_bf16 v[48:51], v[180:183], v[216:219], v[48:51]
	v_exp_f32_e32 v71, v71
	v_mfma_f32_16x16x32_bf16 v[52:55], v[180:183], v[238:241], v[52:55]
	v_add_f32_e32 v220, v64, v65
	ds_read_b128 v[180:183], v210 offset:53248
	s_waitcnt lgkmcnt(6)
	v_mfma_f32_16x16x32_bf16 v[76:79], v[230:233], v[124:127], v[76:79]
	v_add_f32_e32 v221, v68, v69
	v_mfma_f32_16x16x32_bf16 v[72:75], v[230:233], v[108:111], v[72:75]
	v_add_f32_e32 v220, v220, v66
	ds_read_b128 v[230:233], v246 offset:8192
	v_mfma_f32_16x16x32_bf16 v[60:63], v[234:237], v[238:241], v[60:63]
	v_add_f32_e32 v221, v221, v70
	v_add_f32_e32 v220, v220, v67
	v_mfma_f32_16x16x32_bf16 v[56:59], v[234:237], v[216:219], v[56:59]
	v_add_f32_e32 v221, v221, v71
	ds_read_b128 v[234:237], v210 offset:55296
	s_waitcnt lgkmcnt(6)
	v_mfma_f32_16x16x32_bf16 v[80:83], v[160:163], v[96:99], 0
	v_exp_f32_e32 v72, v72
	v_mfma_f32_16x16x32_bf16 v[84:87], v[160:163], v[112:115], 0
	v_exp_f32_e32 v76, v76
	ds_read_b128 v[160:163], v201 offset:12288
	v_mfma_f32_16x16x32_bf16 v[0:3], v[164:167], v[242:245], v[0:3]
	v_exp_f32_e32 v73, v73
	v_mfma_f32_16x16x32_bf16 v[4:7], v[164:167], v[204:207], v[4:7]
	v_exp_f32_e32 v77, v77
	ds_read_b128 v[164:167], v210 offset:57344
	s_waitcnt lgkmcnt(6)
	v_mfma_f32_16x16x32_bf16 v[84:87], v[168:171], v[116:119], v[84:87]
	v_exp_f32_e32 v74, v74
	v_mfma_f32_16x16x32_bf16 v[80:83], v[168:171], v[100:103], v[80:83]
	v_exp_f32_e32 v78, v78
	ds_read_b128 v[168:171], v202 offset:12288
	v_mfma_f32_16x16x32_bf16 v[12:15], v[172:175], v[204:207], v[12:15]
	v_exp_f32_e32 v75, v75
	v_mfma_f32_16x16x32_bf16 v[8:11], v[172:175], v[242:245], v[8:11]
	v_exp_f32_e32 v79, v79
	ds_read_b128 v[172:175], v210 offset:59392
	s_waitcnt lgkmcnt(6)
	v_mfma_f32_16x16x32_bf16 v[80:83], v[176:179], v[104:107], v[80:83]
	v_add_f32_e32 v220, v220, v72
	v_add_f32_e32 v221, v221, v76
	v_mfma_f32_16x16x32_bf16 v[84:87], v[176:179], v[120:123], v[84:87]
	v_add_f32_e32 v220, v220, v73
	ds_read_b128 v[176:179], v203 offset:12288
	s_add_u32 s10, s10, 0x200
	s_addc_u32 s11, s11, 0
	s_add_u32 s12, s12, 0x40000
	s_addc_u32 s13, s13, 0
	s_add_i32 s4, s4, 4
	s_cmpk_lt_u32 s4, 0x104
	s_cselect_b64 s[6:7], -1, 0
	s_and_b64 s[6:7], s[0:1], s[6:7]
	s_and_b64 vcc, exec, s[6:7]
	v_mfma_f32_16x16x32_bf16 v[16:19], v[180:183], v[242:245], v[16:19]
	v_add_f32_e32 v221, v221, v77
	v_add_f32_e32 v220, v220, v74
	v_mfma_f32_16x16x32_bf16 v[20:23], v[180:183], v[204:207], v[20:23]
	v_add_f32_e32 v221, v221, v78
	ds_read_b128 v[180:183], v210 offset:61440
	s_waitcnt lgkmcnt(6)
	v_mfma_f32_16x16x32_bf16 v[84:87], v[230:233], v[124:127], v[84:87]
	v_add_f32_e32 v220, v220, v75
	v_add_f32_e32 v221, v221, v79
	v_mfma_f32_16x16x32_bf16 v[80:83], v[230:233], v[108:111], v[80:83]
	v_cvt_pk_bf16_f32 v216, v64, v65
	ds_read_b128 v[230:233], v246 offset:12288
	v_mfma_f32_16x16x32_bf16 v[28:31], v[234:237], v[204:207], v[28:31]
	v_cvt_pk_bf16_f32 v217, v66, v67
	v_cvt_pk_bf16_f32 v238, v68, v69
	v_mfma_f32_16x16x32_bf16 v[24:27], v[234:237], v[242:245], v[24:27]
	v_cvt_pk_bf16_f32 v239, v70, v71
	ds_read_b128 v[234:237], v210 offset:63488
	s_waitcnt lgkmcnt(6)
	v_mfma_f32_16x16x32_bf16 v[88:91], v[160:163], v[96:99], 0
	v_exp_f32_e32 v80, v80
	v_mfma_f32_16x16x32_bf16 v[92:95], v[160:163], v[112:115], 0
	v_exp_f32_e32 v84, v84
	v_mfma_f32_16x16x32_bf16 v[32:35], v[164:167], v[242:245], v[32:35]
	v_exp_f32_e32 v81, v81
	v_mfma_f32_16x16x32_bf16 v[36:39], v[164:167], v[204:207], v[36:39]
	v_exp_f32_e32 v85, v85
	s_waitcnt lgkmcnt(4)
	v_mfma_f32_16x16x32_bf16 v[92:95], v[168:171], v[116:119], v[92:95]
	v_exp_f32_e32 v82, v82
	v_mfma_f32_16x16x32_bf16 v[88:91], v[168:171], v[100:103], v[88:91]
	v_exp_f32_e32 v86, v86
	v_mfma_f32_16x16x32_bf16 v[44:47], v[172:175], v[204:207], v[44:47]
	v_exp_f32_e32 v83, v83
	v_mfma_f32_16x16x32_bf16 v[40:43], v[172:175], v[242:245], v[40:43]
	v_exp_f32_e32 v87, v87
	s_waitcnt lgkmcnt(3)
	v_mfma_f32_16x16x32_bf16 v[88:91], v[176:179], v[104:107], v[88:91]
	v_add_f32_e32 v220, v220, v80
	v_add_f32_e32 v221, v221, v84
	v_mfma_f32_16x16x32_bf16 v[92:95], v[176:179], v[120:123], v[92:95]
	v_add_f32_e32 v220, v220, v81
	s_waitcnt lgkmcnt(0)
	s_barrier
	ds_read_b128 v[160:163], v201 offset:16384
	ds_read_b128 v[164:167], v209 offset:0
	ds_read_b128 v[168:171], v202 offset:16384
	ds_read_b128 v[172:175], v209 offset:2048
	ds_read_b128 v[176:179], v203 offset:16384
	v_mfma_f32_16x16x32_bf16 v[48:51], v[180:183], v[242:245], v[48:51]
	v_add_f32_e32 v221, v221, v85
	v_add_f32_e32 v220, v220, v82
	v_mfma_f32_16x16x32_bf16 v[52:55], v[180:183], v[204:207], v[52:55]
	v_add_f32_e32 v221, v221, v86
	ds_read_b128 v[180:183], v209 offset:4096
	v_mfma_f32_16x16x32_bf16 v[92:95], v[230:233], v[124:127], v[92:95]
	v_add_f32_e32 v220, v220, v83
	v_add_f32_e32 v221, v221, v87
	v_mfma_f32_16x16x32_bf16 v[88:91], v[230:233], v[108:111], v[88:91]
	v_cvt_pk_bf16_f32 v218, v72, v73
	ds_read_b128 v[230:233], v246 offset:16384
	v_mfma_f32_16x16x32_bf16 v[60:63], v[234:237], v[204:207], v[60:63]
	v_cvt_pk_bf16_f32 v219, v74, v75
	v_cvt_pk_bf16_f32 v240, v76, v77
	v_mfma_f32_16x16x32_bf16 v[56:59], v[234:237], v[242:245], v[56:59]
	v_cvt_pk_bf16_f32 v241, v78, v79
	ds_read_b128 v[234:237], v209 offset:6144
	s_cbranch_vccnz .LBB0_734
	s_setprio 0
	s_waitcnt vmcnt(0)
	s_nop 7
	s_nop 7
	ds_swizzle_b32 v64, v194 offset:swizzle(SWAP,16)
	s_waitcnt lgkmcnt(0)
	v_add_f32_e32 v194, v194, v64
	v_mov_b32_e32 v65, v194
	s_nop 1
	v_permlane32_swap_b32_e32 v194, v65
	v_add_f32_e32 v194, v194, v65
	s_nop 0
	v_rcp_f32_e32 v66, v194
	ds_swizzle_b32 v64, v195 offset:swizzle(SWAP,16)
	s_waitcnt lgkmcnt(0)
	v_add_f32_e32 v195, v195, v64
	v_mov_b32_e32 v65, v195
	s_nop 1
	v_permlane32_swap_b32_e32 v195, v65
	v_add_f32_e32 v195, v195, v65
	s_nop 0
	v_rcp_f32_e32 v67, v195
	v_readlane_b32 s100, v250, 8
	v_mbcnt_lo_u32_b32 v68, -1, 0
	v_mbcnt_hi_u32_b32 v68, -1, v68
	v_and_b32_e32 v69, 15, v68
	v_lshrrev_b32_e32 v70, 4, v68
	s_lshr_b32 s101, s100, 1
	v_add_u32_e32 v69, s101, v69
	v_lshlrev_b32_e32 v69, 12, v69
	v_and_b32_e32 v71, 1, v70
	v_lshlrev_b32_e32 v71, 5, v71
	v_and_b32_e32 v70, 2, v70
	v_lshl_add_u32 v71, v70, 3, v71
	v_add_u32_e32 v70, v69, v71
	v_add_u32_e32 v71, 0x10000, v70
	v_mul_f32_e32 v0, v0, v66
	v_mul_f32_e32 v1, v1, v66
	v_mul_f32_e32 v2, v2, v66
	v_mul_f32_e32 v3, v3, v66
	v_mul_f32_e32 v8, v8, v66
	v_mul_f32_e32 v9, v9, v66
	v_mul_f32_e32 v10, v10, v66
	v_mul_f32_e32 v11, v11, v66
	v_cvt_pk_bf16_f32 v72, v0, v1
	v_cvt_pk_bf16_f32 v73, v2, v3
	v_cvt_pk_bf16_f32 v74, v8, v9
	v_cvt_pk_bf16_f32 v75, v10, v11
	s_nop 1
	v_permlane16_swap_b32_e32 v72, v74
	v_permlane16_swap_b32_e32 v73, v75
	s_nop 1
	global_store_dwordx4 v70, v[72:75], s[58:59] offset:0
	v_mul_f32_e32 v16, v16, v66
	v_mul_f32_e32 v17, v17, v66
	v_mul_f32_e32 v18, v18, v66
	v_mul_f32_e32 v19, v19, v66
	v_mul_f32_e32 v24, v24, v66
	v_mul_f32_e32 v25, v25, v66
	v_mul_f32_e32 v26, v26, v66
	v_mul_f32_e32 v27, v27, v66
	v_cvt_pk_bf16_f32 v76, v16, v17
	v_cvt_pk_bf16_f32 v77, v18, v19
	v_cvt_pk_bf16_f32 v78, v24, v25
	v_cvt_pk_bf16_f32 v79, v26, v27
	s_nop 1
	v_permlane16_swap_b32_e32 v76, v78
	v_permlane16_swap_b32_e32 v77, v79
	s_nop 1
	global_store_dwordx4 v70, v[76:79], s[58:59] offset:64
	v_mul_f32_e32 v32, v32, v66
	v_mul_f32_e32 v33, v33, v66
	v_mul_f32_e32 v34, v34, v66
	v_mul_f32_e32 v35, v35, v66
	v_mul_f32_e32 v40, v40, v66
	v_mul_f32_e32 v41, v41, v66
	v_mul_f32_e32 v42, v42, v66
	v_mul_f32_e32 v43, v43, v66
	v_cvt_pk_bf16_f32 v80, v32, v33
	v_cvt_pk_bf16_f32 v81, v34, v35
	v_cvt_pk_bf16_f32 v82, v40, v41
	v_cvt_pk_bf16_f32 v83, v42, v43
	s_nop 1
	v_permlane16_swap_b32_e32 v80, v82
	v_permlane16_swap_b32_e32 v81, v83
	s_nop 1
	global_store_dwordx4 v70, v[80:83], s[58:59] offset:128
	v_mul_f32_e32 v48, v48, v66
	v_mul_f32_e32 v49, v49, v66
	v_mul_f32_e32 v50, v50, v66
	v_mul_f32_e32 v51, v51, v66
	v_mul_f32_e32 v56, v56, v66
	v_mul_f32_e32 v57, v57, v66
	v_mul_f32_e32 v58, v58, v66
	v_mul_f32_e32 v59, v59, v66
	v_cvt_pk_bf16_f32 v84, v48, v49
	v_cvt_pk_bf16_f32 v85, v50, v51
	v_cvt_pk_bf16_f32 v86, v56, v57
	v_cvt_pk_bf16_f32 v87, v58, v59
	s_nop 1
	v_permlane16_swap_b32_e32 v84, v86
	v_permlane16_swap_b32_e32 v85, v87
	s_nop 1
	global_store_dwordx4 v70, v[84:87], s[58:59] offset:192
	v_mul_f32_e32 v4, v4, v67
	v_mul_f32_e32 v5, v5, v67
	v_mul_f32_e32 v6, v6, v67
	v_mul_f32_e32 v7, v7, v67
	v_mul_f32_e32 v12, v12, v67
	v_mul_f32_e32 v13, v13, v67
	v_mul_f32_e32 v14, v14, v67
	v_mul_f32_e32 v15, v15, v67
	v_cvt_pk_bf16_f32 v88, v4, v5
	v_cvt_pk_bf16_f32 v89, v6, v7
	v_cvt_pk_bf16_f32 v90, v12, v13
	v_cvt_pk_bf16_f32 v91, v14, v15
	s_nop 1
	v_permlane16_swap_b32_e32 v88, v90
	v_permlane16_swap_b32_e32 v89, v91
	s_nop 1
	global_store_dwordx4 v71, v[88:91], s[58:59] offset:0
	v_mul_f32_e32 v20, v20, v67
	v_mul_f32_e32 v21, v21, v67
	v_mul_f32_e32 v22, v22, v67
	v_mul_f32_e32 v23, v23, v67
	v_mul_f32_e32 v28, v28, v67
	v_mul_f32_e32 v29, v29, v67
	v_mul_f32_e32 v30, v30, v67
	v_mul_f32_e32 v31, v31, v67
	v_cvt_pk_bf16_f32 v92, v20, v21
	v_cvt_pk_bf16_f32 v93, v22, v23
	v_cvt_pk_bf16_f32 v94, v28, v29
	v_cvt_pk_bf16_f32 v95, v30, v31
	s_nop 1
	v_permlane16_swap_b32_e32 v92, v94
	v_permlane16_swap_b32_e32 v93, v95
	s_nop 1
	global_store_dwordx4 v71, v[92:95], s[58:59] offset:64
	v_mul_f32_e32 v36, v36, v67
	v_mul_f32_e32 v37, v37, v67
	v_mul_f32_e32 v38, v38, v67
	v_mul_f32_e32 v39, v39, v67
	v_mul_f32_e32 v44, v44, v67
	v_mul_f32_e32 v45, v45, v67
	v_mul_f32_e32 v46, v46, v67
	v_mul_f32_e32 v47, v47, v67
	v_cvt_pk_bf16_f32 v72, v36, v37
	v_cvt_pk_bf16_f32 v73, v38, v39
	v_cvt_pk_bf16_f32 v74, v44, v45
	v_cvt_pk_bf16_f32 v75, v46, v47
	s_nop 1
	v_permlane16_swap_b32_e32 v72, v74
	v_permlane16_swap_b32_e32 v73, v75
	s_nop 1
	global_store_dwordx4 v71, v[72:75], s[58:59] offset:128
	v_mul_f32_e32 v52, v52, v67
	v_mul_f32_e32 v53, v53, v67
	v_mul_f32_e32 v54, v54, v67
	v_mul_f32_e32 v55, v55, v67
	v_mul_f32_e32 v60, v60, v67
	v_mul_f32_e32 v61, v61, v67
	v_mul_f32_e32 v62, v62, v67
	v_mul_f32_e32 v63, v63, v67
	v_cvt_pk_bf16_f32 v76, v52, v53
	v_cvt_pk_bf16_f32 v77, v54, v55
	v_cvt_pk_bf16_f32 v78, v60, v61
	v_cvt_pk_bf16_f32 v79, v62, v63
	s_nop 1
	v_permlane16_swap_b32_e32 v76, v78
	v_permlane16_swap_b32_e32 v77, v79
	s_nop 1
	global_store_dwordx4 v71, v[76:79], s[58:59] offset:192
	s_barrier
